# NSA units remapped so that each XCD works on two (batch,group) pairs (K/V tiles stay L2 resident)
# speedup vs baseline: 1.0010x; 1.0010x over previous
; __global__ void __launch_bounds__(NWAVES * 64, 2) trunk_fwd(Args args) {
;     ...
;             for (int L = bx; L < 512; L += G) { int bg, iq; if (L < 256) { bg = L >> 4; iq = 31 - (L & 15); } else { bg = (L - 256) >> 4; iq = (L - 256) & 15; }
;                 nsa::unit(lds, Zb, KCT, KCT + (size_t)16 * 128 * 64, OA, bg >> 2, bg & 3, iq, tz); }
.LBB0_393:
	s_andn2_b64 vcc, exec, s[0:1]
	s_cbranch_vccnz .LBB0_582
	v_readlane_b32 s0, v252, 2
	v_readlane_b32 s1, v252, 3
	v_mov_b32_e32 v123, v0
	s_andn2_b64 vcc, exec, s[0:1]
	v_readlane_b32 s0, v254, 40
	s_lshr_b32 s20, s0, 3
	s_and_b32 s21, s0, 7
	s_lshl_b32 s21, s21, 5
	s_or_b32 s21, s21, s20
	s_cmpk_eq_i32 s33, 0x100
	s_cselect_b32 s21, s21, s0
	v_readfirstlane_b32 s20, v123
	v_readlane_b32 s1, v254, 41
	s_cbranch_vccz .LBB0_412
